# stack3: stack1 + QKV small column pass reads its A fragments from LDS one k-step ahead (two register sets)
# speedup vs baseline: 1.0053x; 1.0053x over previous
; #define LOADP(i_, ks_) do { pa[i_] = *(const bf16x8*)(wb + (size_t)((ks_) * 144) * 1024 + voff); pb[i_] = *(const bf16x8*)(wb + (size_t)((ks_) * 144 + 2) * 1024 + voff); } while (0)
; DEVINL void phase2(const Params& P, unsigned char* smem, XPre& X, const bool have_pre) {
;     ...
;             const int slot = 32 + (wv >> 1), fr0 = wv & 1;
;             const unsigned char* wb = (const unsigned char*)(P.ws + WS_WQF) + (size_t)(4 * slot + fr0) * 1024;
;             bf16x8 pa[4], pb[4];
;     ...
;             LOADP(0, 0); LOADP(1, 1); LOADP(2, 2);
.LBB0_191:
	v_sub_co_u32_e64 v2, s[0:1], s85, 1
	s_and_b64 s[0:1], s[0:1], exec
	v_readfirstlane_b32 s0, v2
	s_cselect_b32 s6, 2, s0
	s_and_b64 s[0:1], s[20:21], exec
	s_cselect_b32 s8, s85, s6
	s_cmp_gt_i32 s8, 1
	s_mov_b64 s[0:1], -1
	s_cbranch_scc0 .LBB0_203
	global_load_dwordx4 v[38:41], v[184:185], off
	global_load_dwordx4 v[42:45], v[184:185], off offset:2048
	global_load_dwordx4 v[18:21], v[186:187], off
	global_load_dwordx4 v[22:25], v[188:189], off
	global_load_dwordx4 v[26:29], v[190:191], off
	global_load_dwordx4 v[34:37], v[192:193], off
	v_mov_b32_e32 v2, 0
	s_mov_b32 s6, 0
	s_mov_b64 s[0:1], 0
	v_mov_b32_e32 v58, v216
	v_mov_b32_e32 v3, v2
	v_mov_b32_e32 v4, v2
	v_mov_b32_e32 v5, v2
	v_mov_b32_e32 v10, v2
	v_mov_b32_e32 v11, v2
	v_mov_b32_e32 v12, v2
	v_mov_b32_e32 v13, v2
	v_mov_b32_e32 v30, v2
	v_mov_b32_e32 v31, v2
	v_mov_b32_e32 v32, v2
	v_mov_b32_e32 v33, v2
	v_mov_b32_e32 v50, v2
	v_mov_b32_e32 v51, v2
	v_mov_b32_e32 v52, v2
	v_mov_b32_e32 v53, v2
	v_mov_b32_e32 v6, v2
	v_mov_b32_e32 v7, v2
	v_mov_b32_e32 v8, v2
	v_mov_b32_e32 v9, v2
	v_mov_b32_e32 v14, v2
	v_mov_b32_e32 v15, v2
	v_mov_b32_e32 v16, v2
	v_mov_b32_e32 v17, v2
	v_mov_b32_e32 v46, v2
	v_mov_b32_e32 v47, v2
	v_mov_b32_e32 v48, v2
	v_mov_b32_e32 v49, v2
	v_mov_b32_e32 v54, v2
	v_mov_b32_e32 v55, v2
	v_mov_b32_e32 v56, v2
	v_mov_b32_e32 v57, v2
	v_add_u32_e32 v104, -8, v58
	v_xor_b32_e32 v104, v104, v181
	v_lshl_add_u32 v104, v104, 4, v212
	v_add_u32_e32 v105, 0x10000, v104
	ds_read_b128 v[68:71], v104
	ds_read_b128 v[72:75], v104 offset:32768
	ds_read_b128 v[76:79], v105
	ds_read_b128 v[80:83], v105 offset:32768
; #define LOADP(i_, ks_) do { pa[i_] = *(const bf16x8*)(wb + (size_t)((ks_) * 144) * 1024 + voff); pb[i_] = *(const bf16x8*)(wb + (size_t)((ks_) * 144 + 2) * 1024 + voff); } while (0)
; #define STEP(i_, ks_) do { _Pragma("unroll") for (int mi = 0; mi < 4; ++mi) { const bf16x8 f = AFRAG(mi, ks_); \
;         acc[0][mi] = __builtin_amdgcn_mfma_f32_16x16x32_bf16(pa[i_], f, acc[0][mi], 0, 0, 0); acc[1][mi] = __builtin_amdgcn_mfma_f32_16x16x32_bf16(pb[i_], f, acc[1][mi], 0, 0, 0); } } while (0)
; DEVINL void phase2(const Params& P, unsigned char* smem, XPre& X, const bool have_pre) {
;     ...
;             LOADP(0, 0); LOADP(1, 1); LOADP(2, 2);
; #pragma unroll 1
;             for (int ks = 0; ks < 32; ks += 4) {
;                 LOADP(3, ks + 3);                            __builtin_amdgcn_sched_barrier(0);
;                 STEP(0, ks);     __builtin_amdgcn_sched_barrier(0); LOADP(0, ks + 4 < 32 ? ks + 4 : 31); __builtin_amdgcn_sched_barrier(0);
;                 STEP(1, ks + 1); __builtin_amdgcn_sched_barrier(0); LOADP(1, ks + 5 < 32 ? ks + 5 : 31); __builtin_amdgcn_sched_barrier(0);
;                 STEP(2, ks + 2); __builtin_amdgcn_sched_barrier(0); LOADP(2, ks + 6 < 32 ? ks + 6 : 31); __builtin_amdgcn_sched_barrier(0);
;                 STEP(3, ks + 3); __builtin_amdgcn_sched_barrier(0);
;             }
.LBB0_193:
	v_lshl_add_u64 v[60:61], v[196:197], 0, s[0:1]
	s_mov_b32 s7, 0x46c000
	v_add_co_u32_e32 v64, vcc, s7, v60
	s_nop 1
	v_addc_co_u32_e32 v65, vcc, 0, v61, vcc
	global_load_dwordx4 v[60:63], v[64:65], off
	s_nop 0
	global_load_dwordx4 v[64:67], v[64:65], off offset:2048
	v_add_u32_e32 v104, -4, v58
	v_xor_b32_e32 v104, v104, v181
	v_lshl_add_u32 v104, v104, 4, v212
	v_add_u32_e32 v105, 0x10000, v104
	ds_read_b128 v[86:89], v104
	ds_read_b128 v[90:93], v104 offset:32768
	ds_read_b128 v[94:97], v105
	ds_read_b128 v[98:101], v105 offset:32768
	s_waitcnt vmcnt(7) lgkmcnt(7)
	v_mfma_f32_16x16x32_bf16 v[54:57], v[38:41], v[68:71], v[54:57]
	s_waitcnt vmcnt(6)
	v_mfma_f32_16x16x32_bf16 v[50:53], v[42:45], v[68:71], v[50:53]
	s_waitcnt lgkmcnt(6)
	v_mfma_f32_16x16x32_bf16 v[46:49], v[38:41], v[72:75], v[46:49]
	v_mfma_f32_16x16x32_bf16 v[30:33], v[42:45], v[72:75], v[30:33]
	s_waitcnt lgkmcnt(5)
	v_mfma_f32_16x16x32_bf16 v[14:17], v[38:41], v[76:79], v[14:17]
	v_mfma_f32_16x16x32_bf16 v[10:13], v[42:45], v[76:79], v[10:13]
	s_waitcnt lgkmcnt(4)
	v_mfma_f32_16x16x32_bf16 v[6:9], v[38:41], v[80:83], v[6:9]
	v_mfma_f32_16x16x32_bf16 v[2:5], v[42:45], v[80:83], v[2:5]
	s_add_i32 s7, s6, 4
	s_add_u32 s0, s0, 0x90000
	s_addc_u32 s1, s1, 0
	s_cmp_lt_u32 s6, 28
	s_cselect_b32 s18, s0, 0x45c000
	v_lshl_add_u64 v[42:43], v[184:185], 0, s[18:19]
	global_load_dwordx4 v[38:41], v[42:43], off
	s_nop 0
	global_load_dwordx4 v[42:45], v[42:43], off offset:2048
	s_min_u32 s9, s6, 26
	s_mul_i32 s9, s9, 0x24000
	s_add_u32 s10, s58, s9
	s_addc_u32 s11, s59, 0
	s_min_u32 s9, s6, 25
	s_mul_i32 s9, s9, 0x24000
	s_add_u32 s12, s58, s9
	s_addc_u32 s13, s59, 0
	s_cmp_gt_u32 s6, 27
	v_xor_b32_e32 v104, v58, v181
	v_lshl_add_u32 v104, v104, 4, v212
	v_add_u32_e32 v105, 0x10000, v104
	ds_read_b128 v[68:71], v104
	ds_read_b128 v[72:75], v104 offset:32768
	ds_read_b128 v[76:79], v105
	ds_read_b128 v[80:83], v105 offset:32768
	s_waitcnt vmcnt(7) lgkmcnt(7)
	v_mfma_f32_16x16x32_bf16 v[54:57], v[18:21], v[86:89], v[54:57]
	s_waitcnt vmcnt(6)
	v_mfma_f32_16x16x32_bf16 v[50:53], v[22:25], v[86:89], v[50:53]
	s_waitcnt lgkmcnt(6)
	v_mfma_f32_16x16x32_bf16 v[46:49], v[18:21], v[90:93], v[46:49]
	v_mfma_f32_16x16x32_bf16 v[30:33], v[22:25], v[90:93], v[30:33]
	s_waitcnt lgkmcnt(5)
	v_mfma_f32_16x16x32_bf16 v[14:17], v[18:21], v[94:97], v[14:17]
	v_mfma_f32_16x16x32_bf16 v[10:13], v[22:25], v[94:97], v[10:13]
	s_waitcnt lgkmcnt(4)
	v_mfma_f32_16x16x32_bf16 v[6:9], v[18:21], v[98:101], v[6:9]
	v_mfma_f32_16x16x32_bf16 v[2:5], v[22:25], v[98:101], v[2:5]
	v_lshl_add_u64 v[18:19], s[10:11], 0, v[182:183]
	s_mov_b32 s6, 0xb4000
	v_add_co_u32_e32 v22, vcc, s6, v18
	s_nop 1
	v_addc_co_u32_e32 v23, vcc, 0, v19, vcc
	global_load_dwordx4 v[18:21], v[22:23], off
	s_nop 0
	global_load_dwordx4 v[22:25], v[22:23], off offset:2048
	v_add_u32_e32 v104, 4, v58
	v_xor_b32_e32 v104, v104, v181
	v_lshl_add_u32 v104, v104, 4, v212
	v_add_u32_e32 v105, 0x10000, v104
	ds_read_b128 v[86:89], v104
	ds_read_b128 v[90:93], v104 offset:32768
	ds_read_b128 v[94:97], v105
	ds_read_b128 v[98:101], v105 offset:32768
	s_waitcnt vmcnt(7) lgkmcnt(7)
	v_mfma_f32_16x16x32_bf16 v[54:57], v[26:29], v[68:71], v[54:57]
	s_waitcnt vmcnt(6)
	v_mfma_f32_16x16x32_bf16 v[50:53], v[34:37], v[68:71], v[50:53]
	s_waitcnt lgkmcnt(6)
	v_mfma_f32_16x16x32_bf16 v[46:49], v[26:29], v[72:75], v[46:49]
	v_mfma_f32_16x16x32_bf16 v[30:33], v[34:37], v[72:75], v[30:33]
	s_waitcnt lgkmcnt(5)
	v_mfma_f32_16x16x32_bf16 v[14:17], v[26:29], v[76:79], v[14:17]
	v_mfma_f32_16x16x32_bf16 v[10:13], v[34:37], v[76:79], v[10:13]
	s_waitcnt lgkmcnt(4)
	v_mfma_f32_16x16x32_bf16 v[6:9], v[26:29], v[80:83], v[6:9]
	v_mfma_f32_16x16x32_bf16 v[2:5], v[34:37], v[80:83], v[2:5]
	v_lshl_add_u64 v[26:27], s[12:13], 0, v[182:183]
	s_mov_b32 s6, 0xd8000
	v_add_co_u32_e32 v34, vcc, s6, v26
	s_nop 1
	v_addc_co_u32_e32 v35, vcc, 0, v27, vcc
	global_load_dwordx4 v[26:29], v[34:35], off
	s_nop 0
	global_load_dwordx4 v[34:37], v[34:35], off offset:2048
	v_add_u32_e32 v58, 16, v58
	v_add_u32_e32 v104, -8, v58
	v_xor_b32_e32 v104, v104, v181
	v_lshl_add_u32 v104, v104, 4, v212
	v_add_u32_e32 v105, 0x10000, v104
	ds_read_b128 v[68:71], v104
	ds_read_b128 v[72:75], v104 offset:32768
	ds_read_b128 v[76:79], v105
	ds_read_b128 v[80:83], v105 offset:32768
	s_waitcnt vmcnt(7) lgkmcnt(7)
	v_mfma_f32_16x16x32_bf16 v[54:57], v[60:63], v[86:89], v[54:57]
	s_waitcnt vmcnt(6)
	v_mfma_f32_16x16x32_bf16 v[50:53], v[64:67], v[86:89], v[50:53]
	s_waitcnt lgkmcnt(6)
	v_mfma_f32_16x16x32_bf16 v[46:49], v[60:63], v[90:93], v[46:49]
	v_mfma_f32_16x16x32_bf16 v[30:33], v[64:67], v[90:93], v[30:33]
	s_waitcnt lgkmcnt(5)
	v_mfma_f32_16x16x32_bf16 v[14:17], v[60:63], v[94:97], v[14:17]
	v_mfma_f32_16x16x32_bf16 v[10:13], v[64:67], v[94:97], v[10:13]
	s_waitcnt lgkmcnt(4)
	v_mfma_f32_16x16x32_bf16 v[6:9], v[60:63], v[98:101], v[6:9]
	v_mfma_f32_16x16x32_bf16 v[2:5], v[64:67], v[98:101], v[2:5]
	s_mov_b32 s6, s7
	s_cbranch_scc0 .LBB0_193
	s_waitcnt vmcnt(3) lgkmcnt(0)
	v_mov_b32_e32 v20, v180
	s_and_b64 vcc, s[20:21], exec
	s_waitcnt vmcnt(2)
	v_and_or_b32 v24, v20, 15, s62
	v_and_b32_e32 v18, -16, v20
	v_add_u32_e32 v22, s25, v18
	v_add_u32_e32 v23, s81, v18
	v_lshlrev_b32_e32 v178, 7, v24
	s_cbranch_vccz .LBB0_196
	v_add_u32_e32 v18, v23, v178
	s_waitcnt vmcnt(1)
	ds_read_b128 v[26:29], v18
	v_add_u32_e32 v18, v22, v178
	s_waitcnt vmcnt(0)
	ds_read_b128 v[34:37], v18
	s_waitcnt lgkmcnt(1)
	v_pk_mul_f32 v[18:19], v[52:53], v[28:29]
	v_pk_mul_f32 v[38:39], v[50:51], v[26:27]
	s_waitcnt lgkmcnt(0)
	v_pk_fma_f32 v[18:19], v[56:57], v[36:37], v[18:19] neg_lo:[0,0,1] neg_hi:[0,0,1]
	v_pk_fma_f32 v[38:39], v[54:55], v[34:35], v[38:39] neg_lo:[0,0,1] neg_hi:[0,0,1]
	v_pk_mul_f32 v[28:29], v[56:57], v[28:29]
	v_pk_mul_f32 v[26:27], v[54:55], v[26:27]
	v_pk_fma_f32 v[52:53], v[52:53], v[36:37], v[28:29]
	v_pk_fma_f32 v[50:51], v[50:51], v[34:35], v[26:27]
	v_mov_b32_e32 v54, v38
	v_mov_b32_e32 v55, v39
	v_mov_b32_e32 v56, v18
	v_mov_b32_e32 v57, v19
